# v15 + prologue Wc-fold items on the f32 matrix cores: 128 v_mfma_f32_16x16x4_f32 per item (f32 operands, f32 accumulate) instead of VALU fma with uniform LDS lookups
# speedup vs baseline: 1.0010x; 1.0010x over previous
; #define GAS __attribute__((address_space(1)))
; #define LDS_WAIT() asm volatile("s_waitcnt lgkmcnt(0)" ::: "memory")
; __device__ __forceinline__ void p0_prologue(Frame& F) {
;     ...
;         if (r < NI_BD) {
;             const int nb = r & 15, cb = (r >> 4) & 15, part = (r >> 8) & 1, g = r >> 9; const int n = nb * 64 + F.lane, c0 = cb * 8;
;             const GAS float* wsrc = (const GAS float*)inp(F, I_WOUT) + (size_t)(512 + 128 * g) * 1024 + n;
;             { float s0, c0_, s1, c1_; sincospif((float)F.lane * (1.f / 64.f), &s0, &c0_); sincospif((float)(F.lane + 64) * (1.f / 64.f), &s1, &c1_);
;               scr[F.lane] = part ? s0 : c0_; scr[F.lane + 64] = part ? s1 : c1_; LDS_WAIT(); asm volatile("" ::: "memory"); }
;             float acc8[8];
; #pragma unroll
;             for (int j = 0; j < 8; ++j) acc8[j] = 0.f;
; #pragma unroll 2
;             for (int m = 0; m < 128; ++m) { const float wv = wsrc[(size_t)m * 1024];
.Lbd_pipe:
	v_mbcnt_lo_u32_b32 v13, -1, 0
	v_mbcnt_hi_u32_b32 v13, -1, v13
	v_lshrrev_b32_e32 v14, 4, v13
	v_and_b32_e32 v15, 15, v13
	v_mul_u32_u24_e32 v2, 0xfc0, v14
	v_mov_b32_e32 v3, 0
	v_lshl_add_u64 v[4:5], v[4:5], 0, v[2:3]
	s_mov_b64 s[0:1], 0x4000
	v_add_u32_e32 v10, s44, v15
	v_mul_u32_u24_e32 v11, v14, v10
	v_lshlrev_b32_e32 v10, 2, v10
	global_load_dword v120, v[4:5], off offset:-4096
	global_load_dword v121, v[4:5], off offset:-4032
	global_load_dword v122, v[4:5], off offset:-3968
	global_load_dword v123, v[4:5], off offset:-3904
	v_lshl_add_u64 v[4:5], v[4:5], 0, s[0:1]
	global_load_dword v124, v[4:5], off offset:-4096
	global_load_dword v125, v[4:5], off offset:-4032
	global_load_dword v126, v[4:5], off offset:-3968
	global_load_dword v127, v[4:5], off offset:-3904
	v_lshl_add_u64 v[4:5], v[4:5], 0, s[0:1]
	global_load_dword v128, v[4:5], off offset:-4096
	global_load_dword v129, v[4:5], off offset:-4032
	global_load_dword v130, v[4:5], off offset:-3968
	global_load_dword v131, v[4:5], off offset:-3904
	v_lshl_add_u64 v[4:5], v[4:5], 0, s[0:1]
	global_load_dword v132, v[4:5], off offset:-4096
	global_load_dword v133, v[4:5], off offset:-4032
	global_load_dword v134, v[4:5], off offset:-3968
	global_load_dword v135, v[4:5], off offset:-3904
	v_lshl_add_u64 v[4:5], v[4:5], 0, s[0:1]
	global_load_dword v136, v[4:5], off offset:-4096
	global_load_dword v137, v[4:5], off offset:-4032
	global_load_dword v138, v[4:5], off offset:-3968
	global_load_dword v139, v[4:5], off offset:-3904
	v_lshl_add_u64 v[4:5], v[4:5], 0, s[0:1]
	global_load_dword v140, v[4:5], off offset:-4096
	global_load_dword v141, v[4:5], off offset:-4032
	global_load_dword v142, v[4:5], off offset:-3968
	global_load_dword v143, v[4:5], off offset:-3904
	v_lshl_add_u64 v[4:5], v[4:5], 0, s[0:1]
	global_load_dword v144, v[4:5], off offset:-4096
	global_load_dword v145, v[4:5], off offset:-4032
	global_load_dword v146, v[4:5], off offset:-3968
	global_load_dword v147, v[4:5], off offset:-3904
	v_lshl_add_u64 v[4:5], v[4:5], 0, s[0:1]
	global_load_dword v148, v[4:5], off offset:-4096
	global_load_dword v149, v[4:5], off offset:-4032
	global_load_dword v150, v[4:5], off offset:-3968
	global_load_dword v151, v[4:5], off offset:-3904
	v_lshl_add_u64 v[4:5], v[4:5], 0, s[0:1]
	global_load_dword v152, v[4:5], off offset:-4096
	global_load_dword v153, v[4:5], off offset:-4032
	global_load_dword v154, v[4:5], off offset:-3968
	global_load_dword v155, v[4:5], off offset:-3904
	v_lshl_add_u64 v[4:5], v[4:5], 0, s[0:1]
	global_load_dword v156, v[4:5], off offset:-4096
	global_load_dword v157, v[4:5], off offset:-4032
	global_load_dword v158, v[4:5], off offset:-3968
	global_load_dword v159, v[4:5], off offset:-3904
	v_lshl_add_u64 v[4:5], v[4:5], 0, s[0:1]
	global_load_dword v160, v[4:5], off offset:-4096
	global_load_dword v161, v[4:5], off offset:-4032
	global_load_dword v162, v[4:5], off offset:-3968
	global_load_dword v163, v[4:5], off offset:-3904
	v_lshl_add_u64 v[4:5], v[4:5], 0, s[0:1]
	global_load_dword v164, v[4:5], off offset:-4096
	global_load_dword v165, v[4:5], off offset:-4032
	global_load_dword v166, v[4:5], off offset:-3968
	global_load_dword v167, v[4:5], off offset:-3904
	v_lshl_add_u64 v[4:5], v[4:5], 0, s[0:1]
	global_load_dword v168, v[4:5], off offset:-4096
	global_load_dword v169, v[4:5], off offset:-4032
	global_load_dword v170, v[4:5], off offset:-3968
	global_load_dword v171, v[4:5], off offset:-3904
	v_lshl_add_u64 v[4:5], v[4:5], 0, s[0:1]
	global_load_dword v172, v[4:5], off offset:-4096
	global_load_dword v173, v[4:5], off offset:-4032
	global_load_dword v174, v[4:5], off offset:-3968
	global_load_dword v175, v[4:5], off offset:-3904
	v_lshl_add_u64 v[4:5], v[4:5], 0, s[0:1]
	global_load_dword v176, v[4:5], off offset:-4096
	global_load_dword v177, v[4:5], off offset:-4032
	global_load_dword v178, v[4:5], off offset:-3968
	global_load_dword v179, v[4:5], off offset:-3904
	v_lshl_add_u64 v[4:5], v[4:5], 0, s[0:1]
	global_load_dword v180, v[4:5], off offset:-4096
	global_load_dword v181, v[4:5], off offset:-4032
	global_load_dword v182, v[4:5], off offset:-3968
	global_load_dword v183, v[4:5], off offset:-3904
	v_lshl_add_u64 v[4:5], v[4:5], 0, s[0:1]
	v_and_b32_e32 v40, 0x7f, v11
	v_lshl_add_u32 v40, v40, 2, s49
	ds_read_b32 v6, v40
	v_add_u32_e32 v11, v11, v10
	v_and_b32_e32 v40, 0x7f, v11
	v_lshl_add_u32 v40, v40, 2, s49
	ds_read_b32 v7, v40
	v_add_u32_e32 v11, v11, v10
	v_and_b32_e32 v40, 0x7f, v11
	v_lshl_add_u32 v40, v40, 2, s49
	ds_read_b32 v8, v40
	v_add_u32_e32 v11, v11, v10
	v_and_b32_e32 v40, 0x7f, v11
	v_lshl_add_u32 v40, v40, 2, s49
	ds_read_b32 v9, v40
	v_add_u32_e32 v11, v11, v10
	s_waitcnt vmcnt(47)
	global_load_dword v184, v[4:5], off offset:-4096
	global_load_dword v185, v[4:5], off offset:-4032
	global_load_dword v186, v[4:5], off offset:-3968
	global_load_dword v187, v[4:5], off offset:-3904
	v_lshl_add_u64 v[4:5], v[4:5], 0, s[0:1]
	global_load_dword v188, v[4:5], off offset:-4096
	global_load_dword v189, v[4:5], off offset:-4032
	global_load_dword v190, v[4:5], off offset:-3968
	global_load_dword v191, v[4:5], off offset:-3904
	v_lshl_add_u64 v[4:5], v[4:5], 0, s[0:1]
	global_load_dword v192, v[4:5], off offset:-4096
	global_load_dword v193, v[4:5], off offset:-4032
	global_load_dword v194, v[4:5], off offset:-3968
	global_load_dword v195, v[4:5], off offset:-3904
	v_lshl_add_u64 v[4:5], v[4:5], 0, s[0:1]
	global_load_dword v196, v[4:5], off offset:-4096
	global_load_dword v197, v[4:5], off offset:-4032
	global_load_dword v198, v[4:5], off offset:-3968
	global_load_dword v199, v[4:5], off offset:-3904
	v_lshl_add_u64 v[4:5], v[4:5], 0, s[0:1]
	v_and_b32_e32 v40, 0x7f, v11
	v_lshl_add_u32 v40, v40, 2, s49
	ds_read_b32 v2, v40
	v_add_u32_e32 v11, v11, v10
	v_and_b32_e32 v40, 0x7f, v11
	v_lshl_add_u32 v40, v40, 2, s49
	ds_read_b32 v3, v40
	v_add_u32_e32 v11, v11, v10
	v_and_b32_e32 v40, 0x7f, v11
	v_lshl_add_u32 v40, v40, 2, s49
	ds_read_b32 v13, v40
	v_add_u32_e32 v11, v11, v10
	v_and_b32_e32 v40, 0x7f, v11
	v_lshl_add_u32 v40, v40, 2, s49
	ds_read_b32 v17, v40
	v_add_u32_e32 v11, v11, v10
	s_waitcnt lgkmcnt(4)
; __device__ __forceinline__ void p0_prologue(Frame& F) {
;     ...
;             for (int m = 0; m < 128; ++m) { const float wv = wsrc[(size_t)m * 1024];
; #pragma unroll
;                 for (int j = 0; j < 8; ++j) acc8[j] += scr[(m * (c0 + j)) & 127] * wv; }
	v_mfma_f32_16x16x4_f32 v[18:21], v6, v120, 0
	v_mfma_f32_16x16x4_f32 v[22:25], v6, v121, 0
	v_mfma_f32_16x16x4_f32 v[26:29], v6, v122, 0
	v_mfma_f32_16x16x4_f32 v[30:33], v6, v123, 0
	v_mfma_f32_16x16x4_f32 v[18:21], v7, v124, v[18:21]
	v_mfma_f32_16x16x4_f32 v[22:25], v7, v125, v[22:25]
	v_mfma_f32_16x16x4_f32 v[26:29], v7, v126, v[26:29]
	v_mfma_f32_16x16x4_f32 v[30:33], v7, v127, v[30:33]
	v_mfma_f32_16x16x4_f32 v[18:21], v8, v128, v[18:21]
	v_mfma_f32_16x16x4_f32 v[22:25], v8, v129, v[22:25]
	v_mfma_f32_16x16x4_f32 v[26:29], v8, v130, v[26:29]
	v_mfma_f32_16x16x4_f32 v[30:33], v8, v131, v[30:33]
	v_mfma_f32_16x16x4_f32 v[18:21], v9, v132, v[18:21]
	v_mfma_f32_16x16x4_f32 v[22:25], v9, v133, v[22:25]
	v_mfma_f32_16x16x4_f32 v[26:29], v9, v134, v[26:29]
	v_mfma_f32_16x16x4_f32 v[30:33], v9, v135, v[30:33]
	s_waitcnt vmcnt(47)
	global_load_dword v200, v[4:5], off offset:-4096
	global_load_dword v201, v[4:5], off offset:-4032
	global_load_dword v202, v[4:5], off offset:-3968
	global_load_dword v203, v[4:5], off offset:-3904
	v_lshl_add_u64 v[4:5], v[4:5], 0, s[0:1]
	global_load_dword v204, v[4:5], off offset:-4096
	global_load_dword v205, v[4:5], off offset:-4032
	global_load_dword v206, v[4:5], off offset:-3968
	global_load_dword v207, v[4:5], off offset:-3904
	v_lshl_add_u64 v[4:5], v[4:5], 0, s[0:1]
	global_load_dword v208, v[4:5], off offset:-4096
	global_load_dword v209, v[4:5], off offset:-4032
	global_load_dword v210, v[4:5], off offset:-3968
	global_load_dword v211, v[4:5], off offset:-3904
	v_lshl_add_u64 v[4:5], v[4:5], 0, s[0:1]
	global_load_dword v212, v[4:5], off offset:-4096
	global_load_dword v213, v[4:5], off offset:-4032
	global_load_dword v214, v[4:5], off offset:-3968
	global_load_dword v215, v[4:5], off offset:-3904
	v_lshl_add_u64 v[4:5], v[4:5], 0, s[0:1]
	v_and_b32_e32 v40, 0x7f, v11
	v_lshl_add_u32 v40, v40, 2, s49
	ds_read_b32 v6, v40
	v_add_u32_e32 v11, v11, v10
	v_and_b32_e32 v40, 0x7f, v11
	v_lshl_add_u32 v40, v40, 2, s49
	ds_read_b32 v7, v40
	v_add_u32_e32 v11, v11, v10
	v_and_b32_e32 v40, 0x7f, v11
	v_lshl_add_u32 v40, v40, 2, s49
	ds_read_b32 v8, v40
	v_add_u32_e32 v11, v11, v10
	v_and_b32_e32 v40, 0x7f, v11
	v_lshl_add_u32 v40, v40, 2, s49
	ds_read_b32 v9, v40
	v_add_u32_e32 v11, v11, v10
	s_waitcnt lgkmcnt(4)
	v_mfma_f32_16x16x4_f32 v[18:21], v2, v136, v[18:21]
	v_mfma_f32_16x16x4_f32 v[22:25], v2, v137, v[22:25]
	v_mfma_f32_16x16x4_f32 v[26:29], v2, v138, v[26:29]
	v_mfma_f32_16x16x4_f32 v[30:33], v2, v139, v[30:33]
	v_mfma_f32_16x16x4_f32 v[18:21], v3, v140, v[18:21]
	v_mfma_f32_16x16x4_f32 v[22:25], v3, v141, v[22:25]
	v_mfma_f32_16x16x4_f32 v[26:29], v3, v142, v[26:29]
	v_mfma_f32_16x16x4_f32 v[30:33], v3, v143, v[30:33]
	v_mfma_f32_16x16x4_f32 v[18:21], v13, v144, v[18:21]
	v_mfma_f32_16x16x4_f32 v[22:25], v13, v145, v[22:25]
	v_mfma_f32_16x16x4_f32 v[26:29], v13, v146, v[26:29]
	v_mfma_f32_16x16x4_f32 v[30:33], v13, v147, v[30:33]
	v_mfma_f32_16x16x4_f32 v[18:21], v17, v148, v[18:21]
	v_mfma_f32_16x16x4_f32 v[22:25], v17, v149, v[22:25]
	v_mfma_f32_16x16x4_f32 v[26:29], v17, v150, v[26:29]
	v_mfma_f32_16x16x4_f32 v[30:33], v17, v151, v[30:33]
	s_waitcnt vmcnt(47)
	global_load_dword v216, v[4:5], off offset:-4096
	global_load_dword v217, v[4:5], off offset:-4032
	global_load_dword v218, v[4:5], off offset:-3968
	global_load_dword v219, v[4:5], off offset:-3904
	v_lshl_add_u64 v[4:5], v[4:5], 0, s[0:1]
	global_load_dword v220, v[4:5], off offset:-4096
	global_load_dword v221, v[4:5], off offset:-4032
	global_load_dword v222, v[4:5], off offset:-3968
	global_load_dword v223, v[4:5], off offset:-3904
	v_lshl_add_u64 v[4:5], v[4:5], 0, s[0:1]
	global_load_dword v224, v[4:5], off offset:-4096
	global_load_dword v225, v[4:5], off offset:-4032
	global_load_dword v226, v[4:5], off offset:-3968
	global_load_dword v227, v[4:5], off offset:-3904
	v_lshl_add_u64 v[4:5], v[4:5], 0, s[0:1]
	global_load_dword v228, v[4:5], off offset:-4096
	global_load_dword v229, v[4:5], off offset:-4032
	global_load_dword v230, v[4:5], off offset:-3968
	global_load_dword v231, v[4:5], off offset:-3904
	v_lshl_add_u64 v[4:5], v[4:5], 0, s[0:1]
	v_and_b32_e32 v40, 0x7f, v11
	v_lshl_add_u32 v40, v40, 2, s49
	ds_read_b32 v2, v40
	v_add_u32_e32 v11, v11, v10
	v_and_b32_e32 v40, 0x7f, v11
	v_lshl_add_u32 v40, v40, 2, s49
	ds_read_b32 v3, v40
	v_add_u32_e32 v11, v11, v10
	v_and_b32_e32 v40, 0x7f, v11
	v_lshl_add_u32 v40, v40, 2, s49
	ds_read_b32 v13, v40
	v_add_u32_e32 v11, v11, v10
	v_and_b32_e32 v40, 0x7f, v11
	v_lshl_add_u32 v40, v40, 2, s49
	ds_read_b32 v17, v40
	v_add_u32_e32 v11, v11, v10
	s_waitcnt lgkmcnt(4)
	v_mfma_f32_16x16x4_f32 v[18:21], v6, v152, v[18:21]
	v_mfma_f32_16x16x4_f32 v[22:25], v6, v153, v[22:25]
	v_mfma_f32_16x16x4_f32 v[26:29], v6, v154, v[26:29]
	v_mfma_f32_16x16x4_f32 v[30:33], v6, v155, v[30:33]
	v_mfma_f32_16x16x4_f32 v[18:21], v7, v156, v[18:21]
	v_mfma_f32_16x16x4_f32 v[22:25], v7, v157, v[22:25]
	v_mfma_f32_16x16x4_f32 v[26:29], v7, v158, v[26:29]
	v_mfma_f32_16x16x4_f32 v[30:33], v7, v159, v[30:33]
	v_mfma_f32_16x16x4_f32 v[18:21], v8, v160, v[18:21]
	v_mfma_f32_16x16x4_f32 v[22:25], v8, v161, v[22:25]
	v_mfma_f32_16x16x4_f32 v[26:29], v8, v162, v[26:29]
	v_mfma_f32_16x16x4_f32 v[30:33], v8, v163, v[30:33]
	v_mfma_f32_16x16x4_f32 v[18:21], v9, v164, v[18:21]
	v_mfma_f32_16x16x4_f32 v[22:25], v9, v165, v[22:25]
	v_mfma_f32_16x16x4_f32 v[26:29], v9, v166, v[26:29]
	v_mfma_f32_16x16x4_f32 v[30:33], v9, v167, v[30:33]
	s_waitcnt vmcnt(47)
; __device__ __forceinline__ void p0_prologue(Frame& F) {
;     ...
;             for (int m = 0; m < 128; ++m) { const float wv = wsrc[(size_t)m * 1024];
; #pragma unroll
;                 for (int j = 0; j < 8; ++j) acc8[j] += scr[(m * (c0 + j)) & 127] * wv; }
	global_load_dword v232, v[4:5], off offset:-4096
	global_load_dword v233, v[4:5], off offset:-4032
	global_load_dword v234, v[4:5], off offset:-3968
	global_load_dword v235, v[4:5], off offset:-3904
	v_lshl_add_u64 v[4:5], v[4:5], 0, s[0:1]
	global_load_dword v236, v[4:5], off offset:-4096
	global_load_dword v237, v[4:5], off offset:-4032
	global_load_dword v238, v[4:5], off offset:-3968
	global_load_dword v239, v[4:5], off offset:-3904
	v_lshl_add_u64 v[4:5], v[4:5], 0, s[0:1]
	global_load_dword v240, v[4:5], off offset:-4096
	global_load_dword v241, v[4:5], off offset:-4032
	global_load_dword v242, v[4:5], off offset:-3968
	global_load_dword v243, v[4:5], off offset:-3904
	v_lshl_add_u64 v[4:5], v[4:5], 0, s[0:1]
	global_load_dword v244, v[4:5], off offset:-4096
	global_load_dword v245, v[4:5], off offset:-4032
	global_load_dword v246, v[4:5], off offset:-3968
	global_load_dword v247, v[4:5], off offset:-3904
	v_and_b32_e32 v40, 0x7f, v11
	v_lshl_add_u32 v40, v40, 2, s49
	ds_read_b32 v6, v40
	v_add_u32_e32 v11, v11, v10
	v_and_b32_e32 v40, 0x7f, v11
	v_lshl_add_u32 v40, v40, 2, s49
	ds_read_b32 v7, v40
	v_add_u32_e32 v11, v11, v10
	v_and_b32_e32 v40, 0x7f, v11
	v_lshl_add_u32 v40, v40, 2, s49
	ds_read_b32 v8, v40
	v_add_u32_e32 v11, v11, v10
	v_and_b32_e32 v40, 0x7f, v11
	v_lshl_add_u32 v40, v40, 2, s49
	ds_read_b32 v9, v40
	v_add_u32_e32 v11, v11, v10
	s_waitcnt lgkmcnt(4)
	v_mfma_f32_16x16x4_f32 v[18:21], v2, v168, v[18:21]
	v_mfma_f32_16x16x4_f32 v[22:25], v2, v169, v[22:25]
	v_mfma_f32_16x16x4_f32 v[26:29], v2, v170, v[26:29]
	v_mfma_f32_16x16x4_f32 v[30:33], v2, v171, v[30:33]
	v_mfma_f32_16x16x4_f32 v[18:21], v3, v172, v[18:21]
	v_mfma_f32_16x16x4_f32 v[22:25], v3, v173, v[22:25]
	v_mfma_f32_16x16x4_f32 v[26:29], v3, v174, v[26:29]
	v_mfma_f32_16x16x4_f32 v[30:33], v3, v175, v[30:33]
	v_mfma_f32_16x16x4_f32 v[18:21], v13, v176, v[18:21]
	v_mfma_f32_16x16x4_f32 v[22:25], v13, v177, v[22:25]
	v_mfma_f32_16x16x4_f32 v[26:29], v13, v178, v[26:29]
	v_mfma_f32_16x16x4_f32 v[30:33], v13, v179, v[30:33]
	v_mfma_f32_16x16x4_f32 v[18:21], v17, v180, v[18:21]
	v_mfma_f32_16x16x4_f32 v[22:25], v17, v181, v[22:25]
	v_mfma_f32_16x16x4_f32 v[26:29], v17, v182, v[26:29]
	v_mfma_f32_16x16x4_f32 v[30:33], v17, v183, v[30:33]
	s_waitcnt vmcnt(48)
	v_and_b32_e32 v40, 0x7f, v11
	v_lshl_add_u32 v40, v40, 2, s49
	ds_read_b32 v2, v40
	v_add_u32_e32 v11, v11, v10
	v_and_b32_e32 v40, 0x7f, v11
	v_lshl_add_u32 v40, v40, 2, s49
	ds_read_b32 v3, v40
	v_add_u32_e32 v11, v11, v10
	v_and_b32_e32 v40, 0x7f, v11
	v_lshl_add_u32 v40, v40, 2, s49
	ds_read_b32 v13, v40
	v_add_u32_e32 v11, v11, v10
	v_and_b32_e32 v40, 0x7f, v11
	v_lshl_add_u32 v40, v40, 2, s49
	ds_read_b32 v17, v40
	v_add_u32_e32 v11, v11, v10
	s_waitcnt lgkmcnt(4)
	v_mfma_f32_16x16x4_f32 v[18:21], v6, v184, v[18:21]
	v_mfma_f32_16x16x4_f32 v[22:25], v6, v185, v[22:25]
	v_mfma_f32_16x16x4_f32 v[26:29], v6, v186, v[26:29]
	v_mfma_f32_16x16x4_f32 v[30:33], v6, v187, v[30:33]
	v_mfma_f32_16x16x4_f32 v[18:21], v7, v188, v[18:21]
	v_mfma_f32_16x16x4_f32 v[22:25], v7, v189, v[22:25]
	v_mfma_f32_16x16x4_f32 v[26:29], v7, v190, v[26:29]
	v_mfma_f32_16x16x4_f32 v[30:33], v7, v191, v[30:33]
	v_mfma_f32_16x16x4_f32 v[18:21], v8, v192, v[18:21]
	v_mfma_f32_16x16x4_f32 v[22:25], v8, v193, v[22:25]
	v_mfma_f32_16x16x4_f32 v[26:29], v8, v194, v[26:29]
	v_mfma_f32_16x16x4_f32 v[30:33], v8, v195, v[30:33]
	v_mfma_f32_16x16x4_f32 v[18:21], v9, v196, v[18:21]
	v_mfma_f32_16x16x4_f32 v[22:25], v9, v197, v[22:25]
	v_mfma_f32_16x16x4_f32 v[26:29], v9, v198, v[26:29]
	v_mfma_f32_16x16x4_f32 v[30:33], v9, v199, v[30:33]
	s_waitcnt vmcnt(32)
	v_and_b32_e32 v40, 0x7f, v11
	v_lshl_add_u32 v40, v40, 2, s49
	ds_read_b32 v6, v40
	v_add_u32_e32 v11, v11, v10
	v_and_b32_e32 v40, 0x7f, v11
	v_lshl_add_u32 v40, v40, 2, s49
	ds_read_b32 v7, v40
	v_add_u32_e32 v11, v11, v10
	v_and_b32_e32 v40, 0x7f, v11
	v_lshl_add_u32 v40, v40, 2, s49
	ds_read_b32 v8, v40
	v_add_u32_e32 v11, v11, v10
	v_and_b32_e32 v40, 0x7f, v11
	v_lshl_add_u32 v40, v40, 2, s49
	ds_read_b32 v9, v40
	v_add_u32_e32 v11, v11, v10
	s_waitcnt lgkmcnt(4)
	v_mfma_f32_16x16x4_f32 v[18:21], v2, v200, v[18:21]
	v_mfma_f32_16x16x4_f32 v[22:25], v2, v201, v[22:25]
	v_mfma_f32_16x16x4_f32 v[26:29], v2, v202, v[26:29]
	v_mfma_f32_16x16x4_f32 v[30:33], v2, v203, v[30:33]
	v_mfma_f32_16x16x4_f32 v[18:21], v3, v204, v[18:21]
	v_mfma_f32_16x16x4_f32 v[22:25], v3, v205, v[22:25]
	v_mfma_f32_16x16x4_f32 v[26:29], v3, v206, v[26:29]
	v_mfma_f32_16x16x4_f32 v[30:33], v3, v207, v[30:33]
	v_mfma_f32_16x16x4_f32 v[18:21], v13, v208, v[18:21]
	v_mfma_f32_16x16x4_f32 v[22:25], v13, v209, v[22:25]
	v_mfma_f32_16x16x4_f32 v[26:29], v13, v210, v[26:29]
	v_mfma_f32_16x16x4_f32 v[30:33], v13, v211, v[30:33]
	v_mfma_f32_16x16x4_f32 v[18:21], v17, v212, v[18:21]
	v_mfma_f32_16x16x4_f32 v[22:25], v17, v213, v[22:25]
	v_mfma_f32_16x16x4_f32 v[26:29], v17, v214, v[26:29]
	v_mfma_f32_16x16x4_f32 v[30:33], v17, v215, v[30:33]
	s_waitcnt vmcnt(16)
	v_and_b32_e32 v40, 0x7f, v11
	v_lshl_add_u32 v40, v40, 2, s49
	ds_read_b32 v2, v40
	v_add_u32_e32 v11, v11, v10
	v_and_b32_e32 v40, 0x7f, v11
	v_lshl_add_u32 v40, v40, 2, s49
	ds_read_b32 v3, v40
	v_add_u32_e32 v11, v11, v10
	v_and_b32_e32 v40, 0x7f, v11
	v_lshl_add_u32 v40, v40, 2, s49
	ds_read_b32 v13, v40
	v_add_u32_e32 v11, v11, v10
	v_and_b32_e32 v40, 0x7f, v11
	v_lshl_add_u32 v40, v40, 2, s49
	ds_read_b32 v17, v40
	v_add_u32_e32 v11, v11, v10
	s_waitcnt lgkmcnt(4)
; #define GAS __attribute__((address_space(1)))
; #define LDS_WAIT() asm volatile("s_waitcnt lgkmcnt(0)" ::: "memory")
; __device__ __forceinline__ unsigned f2bf(float f) { unsigned u = __builtin_bit_cast(unsigned, f); return (u + 0x7fffu + ((u >> 16) & 1u)) >> 16; }
; template <class T> __device__ __forceinline__ T* wsp(const Frame& F, size_t off) { return (T*)(F.ws + off); }
; __device__ __forceinline__ void p0_prologue(Frame& F) {
;     ...
;             LDS_WAIT(); asm volatile("" ::: "memory");
;             unsigned h[8];
; #pragma unroll
;             for (int j = 0; j < 8; ++j) h[j] = f2bf(acc8[j] * 0.08838834764831845f);
;             *(GAS v4u*)(wsp<bf16>(F, WS_W2) + (size_t)n * 1536 + 512 + 256 * g + 128 * part + c0) = (v4u){h[0] | (h[1] << 16), h[2] | (h[3] << 16), h[4] | (h[5] << 16), h[6] | (h[7] << 16)};
	v_mfma_f32_16x16x4_f32 v[18:21], v6, v216, v[18:21]
	v_mfma_f32_16x16x4_f32 v[22:25], v6, v217, v[22:25]
	v_mfma_f32_16x16x4_f32 v[26:29], v6, v218, v[26:29]
	v_mfma_f32_16x16x4_f32 v[30:33], v6, v219, v[30:33]
	v_mfma_f32_16x16x4_f32 v[18:21], v7, v220, v[18:21]
	v_mfma_f32_16x16x4_f32 v[22:25], v7, v221, v[22:25]
	v_mfma_f32_16x16x4_f32 v[26:29], v7, v222, v[26:29]
	v_mfma_f32_16x16x4_f32 v[30:33], v7, v223, v[30:33]
	v_mfma_f32_16x16x4_f32 v[18:21], v8, v224, v[18:21]
	v_mfma_f32_16x16x4_f32 v[22:25], v8, v225, v[22:25]
	v_mfma_f32_16x16x4_f32 v[26:29], v8, v226, v[26:29]
	v_mfma_f32_16x16x4_f32 v[30:33], v8, v227, v[30:33]
	v_mfma_f32_16x16x4_f32 v[18:21], v9, v228, v[18:21]
	v_mfma_f32_16x16x4_f32 v[22:25], v9, v229, v[22:25]
	v_mfma_f32_16x16x4_f32 v[26:29], v9, v230, v[26:29]
	v_mfma_f32_16x16x4_f32 v[30:33], v9, v231, v[30:33]
	s_waitcnt vmcnt(0)
	s_waitcnt lgkmcnt(0)
	v_mfma_f32_16x16x4_f32 v[18:21], v2, v232, v[18:21]
	v_mfma_f32_16x16x4_f32 v[22:25], v2, v233, v[22:25]
	v_mfma_f32_16x16x4_f32 v[26:29], v2, v234, v[26:29]
	v_mfma_f32_16x16x4_f32 v[30:33], v2, v235, v[30:33]
	v_mfma_f32_16x16x4_f32 v[18:21], v3, v236, v[18:21]
	v_mfma_f32_16x16x4_f32 v[22:25], v3, v237, v[22:25]
	v_mfma_f32_16x16x4_f32 v[26:29], v3, v238, v[26:29]
	v_mfma_f32_16x16x4_f32 v[30:33], v3, v239, v[30:33]
	v_mfma_f32_16x16x4_f32 v[18:21], v13, v240, v[18:21]
	v_mfma_f32_16x16x4_f32 v[22:25], v13, v241, v[22:25]
	v_mfma_f32_16x16x4_f32 v[26:29], v13, v242, v[26:29]
	v_mfma_f32_16x16x4_f32 v[30:33], v13, v243, v[30:33]
	v_mfma_f32_16x16x4_f32 v[18:21], v17, v244, v[18:21]
	v_mfma_f32_16x16x4_f32 v[22:25], v17, v245, v[22:25]
	v_mfma_f32_16x16x4_f32 v[26:29], v17, v246, v[26:29]
	v_mfma_f32_16x16x4_f32 v[30:33], v17, v247, v[30:33]
	s_nop 7
	s_nop 3
	v_and_b32_e32 v2, 0xffffffc0, v12
	v_or_b32_e32 v2, v2, v15
	v_mov_b64_e32 v[6:7], s[38:39]
	s_movk_i32 s1, 0xc00
	v_readlane_b32 s0, v255, 21
	v_mad_u64_u32 v[6:7], s[4:5], v2, s1, v[6:7]
	s_and_b32 s42, s29, 0xfffffe00
	s_and_b32 s0, s0, 0x78
	v_lshl_add_u64 v[6:7], v[6:7], 0, s[42:43]
	s_lshl_b32 s42, s7, 8
	v_lshl_add_u64 v[6:7], v[6:7], 0, s[42:43]
	s_lshl_b32 s42, s0, 1
	v_lshl_add_u64 v[6:7], v[6:7], 0, s[42:43]
	v_lshlrev_b32_e32 v2, 3, v14
	v_mov_b32_e32 v3, 0
	v_lshl_add_u64 v[6:7], v[6:7], 0, v[2:3]
	v_add_co_u32_e32 v6, vcc, 0x600000, v6
	v_addc_co_u32_e32 v7, vcc, 0, v7, vcc
	s_mov_b32 s4, 0x3db504f3
	s_mov_b32 s42, 0xc000
	s_mov_b32 exec_hi, 0
	v_mul_f32_e32 v18, s4, v18
	v_mul_f32_e32 v19, s4, v19
	v_mul_f32_e32 v20, s4, v20
	v_mul_f32_e32 v21, s4, v21
	v_bfe_u32 v8, v18, 16, 1
	v_bfe_u32 v9, v19, 16, 1
	v_bfe_u32 v10, v20, 16, 1
	v_bfe_u32 v11, v21, 16, 1
	v_add3_u32 v18, v18, v8, s89
	v_add3_u32 v19, v19, v9, s89
	v_add3_u32 v20, v20, v10, s89
	v_add3_u32 v21, v21, v11, s89
	v_lshrrev_b32_e32 v8, 16, v18
	v_lshrrev_b32_e32 v9, 16, v20
	v_and_or_b32 v2, v19, s92, v8
	v_and_or_b32 v3, v21, s92, v9
	global_store_dwordx2 v[6:7], v[2:3], off offset:1024
	v_lshl_add_u64 v[6:7], v[6:7], 0, s[42:43]
	v_mul_f32_e32 v22, s4, v22
	v_mul_f32_e32 v23, s4, v23
	v_mul_f32_e32 v24, s4, v24
	v_mul_f32_e32 v25, s4, v25
	v_bfe_u32 v8, v22, 16, 1
	v_bfe_u32 v9, v23, 16, 1
	v_bfe_u32 v10, v24, 16, 1
	v_bfe_u32 v11, v25, 16, 1
	v_add3_u32 v22, v22, v8, s89
	v_add3_u32 v23, v23, v9, s89
	v_add3_u32 v24, v24, v10, s89
	v_add3_u32 v25, v25, v11, s89
	v_lshrrev_b32_e32 v8, 16, v22
	v_lshrrev_b32_e32 v9, 16, v24
	v_and_or_b32 v2, v23, s92, v8
	v_and_or_b32 v3, v25, s92, v9
	global_store_dwordx2 v[6:7], v[2:3], off offset:1024
	v_lshl_add_u64 v[6:7], v[6:7], 0, s[42:43]
	v_mul_f32_e32 v26, s4, v26
	v_mul_f32_e32 v27, s4, v27
	v_mul_f32_e32 v28, s4, v28
	v_mul_f32_e32 v29, s4, v29
	v_bfe_u32 v8, v26, 16, 1
	v_bfe_u32 v9, v27, 16, 1
	v_bfe_u32 v10, v28, 16, 1
	v_bfe_u32 v11, v29, 16, 1
	v_add3_u32 v26, v26, v8, s89
	v_add3_u32 v27, v27, v9, s89
	v_add3_u32 v28, v28, v10, s89
	v_add3_u32 v29, v29, v11, s89
	v_lshrrev_b32_e32 v8, 16, v26
	v_lshrrev_b32_e32 v9, 16, v28
	v_and_or_b32 v2, v27, s92, v8
	v_and_or_b32 v3, v29, s92, v9
	global_store_dwordx2 v[6:7], v[2:3], off offset:1024
	v_lshl_add_u64 v[6:7], v[6:7], 0, s[42:43]
	v_mul_f32_e32 v30, s4, v30
	v_mul_f32_e32 v31, s4, v31
	v_mul_f32_e32 v32, s4, v32
	v_mul_f32_e32 v33, s4, v33
	v_bfe_u32 v8, v30, 16, 1
	v_bfe_u32 v9, v31, 16, 1
	v_bfe_u32 v10, v32, 16, 1
	v_bfe_u32 v11, v33, 16, 1
	v_add3_u32 v30, v30, v8, s89
	v_add3_u32 v31, v31, v9, s89
	v_add3_u32 v32, v32, v10, s89
	v_add3_u32 v33, v33, v11, s89
	v_lshrrev_b32_e32 v8, 16, v30
	v_lshrrev_b32_e32 v9, 16, v32
	v_and_or_b32 v2, v31, s92, v8
	v_and_or_b32 v3, v33, s92, v9
	global_store_dwordx2 v[6:7], v[2:3], off offset:1024
	s_mov_b32 exec_hi, -1
	v_readlane_b32 s30, v255, 19
	v_readlane_b32 s31, v255, 20
	s_brev_b32 s44, 1
	v_readlane_b32 s45, v255, 18
	v_readlane_b32 s53, v255, 17
	v_readlane_b32 s63, v255, 16
	v_readlane_b32 s69, v255, 15
	v_readlane_b32 s70, v255, 14
	v_readlane_b32 s76, v255, 13
	s_mov_b32 s79, 0xfe5163ab
	s_mov_b32 s81, 0x3c439041
	s_mov_b32 s88, 0xdb629599
	s_mov_b32 s94, 0xf534ddc0
	s_mov_b32 s97, 0xfc2757d1
